# speedup vs baseline: 1.0016x; 1.0016x over previous
.LBB0_15:
	s_load_dwordx4 s[4:7], s[0:1], 0x0
	s_load_dwordx2 s[10:11], s[0:1], 0x10
	s_lshl_b32 s0, s2, 8
	s_and_b32 s0, s0, 0x700
	s_add_i32 s0, s0, s2
	s_and_b32 s0, s0, 0x3ffff80
	s_and_b32 s1, s2, 0x60
	v_and_b32_e32 v2, 31, v0
	s_or_b32 s0, s1, s0
	v_lshrrev_b32_e32 v1, 6, v0
	v_lshrrev_b32_e32 v92, 6, v0
	v_mov_b32_e32 v93, 0
	v_and_b32_e32 v94, 63, v0
	v_lshlrev_b32_e32 v94, 4, v94
	v_lshl_add_u32 v95, v92, 10, v94
	v_bfe_u32 v38, v0, 5, 1
	v_or_b32_e32 v0, s0, v2
	s_lshr_b32 s0, s2, 1
	s_and_b32 s0, s0, 12
	v_or_b32_e32 v44, s0, v1
	v_lshlrev_b32_e32 v34, 6, v0
	v_bitop3_b32 v39, s0, 7, v1 bitop3:0xc8
	v_and_or_b32 v1, v44, 8, v38
	v_ashrrev_i32_e32 v35, 31, v34
	v_lshlrev_b32_e32 v45, 5, v39
	v_lshlrev_b32_e32 v3, 11, v1
	s_waitcnt lgkmcnt(0)
	v_lshl_add_u64 v[0:1], v[34:35], 2, s[4:5]
	v_lshlrev_b32_e32 v32, 5, v38
	v_mov_b32_e32 v33, 0
	v_lshl_add_u64 v[36:37], v[0:1], 0, v[32:33]
	v_or3_b32 v0, v45, v3, v2
	v_lshlrev_b32_e32 v0, 2, v0
	v_or_b32_e32 v1, 0x1000, v0
	v_or_b32_e32 v2, 0x1400, v0
	v_or_b32_e32 v3, 0x1800, v0
	v_or_b32_e32 v4, 0x1c00, v0
	v_lshlrev_b32_e32 v92, 6, v92
	v_lshl_add_u64 v[90:91], v[92:93], 0, v[36:37]
	global_load_dwordx4 v[28:31], v[90:91], off
	global_load_dwordx4 v[24:27], v[90:91], off offset:16
	global_load_dword v77, v0, s[6:7]
	global_load_dword v78, v0, s[6:7] offset:1024
	global_load_dword v79, v0, s[6:7] offset:2048
	global_load_dword v80, v0, s[6:7] offset:3072
	global_load_dword v81, v1, s[6:7]
	global_load_dword v82, v2, s[6:7]
	global_load_dword v83, v3, s[6:7]
	global_load_dword v84, v4, s[6:7]
	v_or_b32_e32 v1, 0x4000, v0
	v_or_b32_e32 v2, 0x4400, v0
	v_or_b32_e32 v3, 0x4800, v0
	v_or_b32_e32 v4, 0x4c00, v0
	v_or_b32_e32 v5, 0x5000, v0
	v_or_b32_e32 v6, 0x5400, v0
	v_or_b32_e32 v7, 0x5800, v0
	v_or_b32_e32 v8, 0x5c00, v0
	global_load_dword v69, v1, s[6:7]
	global_load_dword v70, v2, s[6:7]
	global_load_dword v71, v3, s[6:7]
	global_load_dword v72, v4, s[6:7]
	global_load_dword v73, v5, s[6:7]
	global_load_dword v74, v6, s[6:7]
	global_load_dword v75, v7, s[6:7]
	global_load_dword v76, v8, s[6:7]
	v_or_b32_e32 v1, 0x8000, v0
	v_or_b32_e32 v2, 0x8400, v0
	v_or_b32_e32 v3, 0x8800, v0
	v_or_b32_e32 v4, 0x8c00, v0
	v_or_b32_e32 v5, 0x9000, v0
	v_or_b32_e32 v6, 0x9400, v0
	v_or_b32_e32 v7, 0x9800, v0
	v_or_b32_e32 v8, 0x9c00, v0
	v_or_b32_e32 v46, 0xc000, v0
	global_load_dword v61, v1, s[6:7]
	global_load_dword v62, v2, s[6:7]
	global_load_dword v63, v3, s[6:7]
	global_load_dword v64, v4, s[6:7]
	global_load_dword v65, v5, s[6:7]
	global_load_dword v66, v6, s[6:7]
	global_load_dword v67, v7, s[6:7]
	global_load_dword v68, v8, s[6:7]
	v_or_b32_e32 v49, 0xc400, v0
	v_or_b32_e32 v50, 0xc800, v0
	v_or_b32_e32 v51, 0xcc00, v0
	v_or_b32_e32 v52, 0xd000, v0
	v_or_b32_e32 v53, 0xd400, v0
	v_or_b32_e32 v54, 0xd800, v0
	v_or_b32_e32 v55, 0xdc00, v0
	global_load_dword v32, v46, s[6:7]
	global_load_dword v35, v49, s[6:7]
	global_load_dword v40, v50, s[6:7]
	global_load_dword v41, v51, s[6:7]
	global_load_dword v42, v52, s[6:7]
	global_load_dword v43, v53, s[6:7]
	global_load_dword v47, v54, s[6:7]
	global_load_dword v48, v55, s[6:7]
	v_lshl_or_b32 v36, v38, 2, v45
	v_cmp_gt_u32_e32 vcc, 8, v44
	v_lshlrev_b32_e32 v85, 2, v36
	v_mov_b32_e32 v44, 0
	v_mov_b32_e32 v46, 0
	v_mov_b32_e32 v50, 0
	v_mov_b32_e32 v45, 0
	v_mov_b32_e32 v49, 0
	v_mov_b32_e32 v51, 0
	v_mov_b32_e32 v53, 0
	v_mov_b32_e32 v52, 0
	v_mov_b32_e32 v54, 0
	v_mov_b32_e32 v55, 0
	v_mov_b32_e32 v57, 0
	v_mov_b32_e32 v56, 0
	v_mov_b32_e32 v58, 0
	v_mov_b32_e32 v59, 0
	v_mov_b32_e32 v60, 0
	v_mov_b64_e32 v[36:37], 0x200000
	s_and_saveexec_b64 s[0:1], vcc
	s_cbranch_execz .Lb0_done
	global_load_dword v44, v85, s[10:11]
	global_load_dword v33, v85, s[10:11] offset:4
	global_load_dword v50, v85, s[10:11] offset:8
	global_load_dword v46, v85, s[10:11] offset:12
	global_load_dword v49, v85, s[10:11] offset:32
	global_load_dword v45, v85, s[10:11] offset:36
	global_load_dword v53, v85, s[10:11] offset:40
	global_load_dword v51, v85, s[10:11] offset:44
	global_load_dword v54, v85, s[10:11] offset:64
	global_load_dword v52, v85, s[10:11] offset:68
	global_load_dword v57, v85, s[10:11] offset:72
	global_load_dword v55, v85, s[10:11] offset:76
	global_load_dword v58, v85, s[10:11] offset:96
	global_load_dword v56, v85, s[10:11] offset:100
	global_load_dword v60, v85, s[10:11] offset:104
	global_load_dword v59, v85, s[10:11] offset:108
	v_mov_b64_e32 v[36:37], 0

.LBB1_20:
	s_add_u32 s45, s12, 0x200000
	s_addc_u32 s46, s13, 0
	s_cmpk_lt_u32 s21, 0x100
	s_cselect_b64 s[22:23], -1, 0
	s_or_b64 s[26:27], s[16:17], s[22:23]
	s_and_b64 s[0:1], s[26:27], exec
	s_cselect_b32 s31, s13, s46
	s_cselect_b32 s34, s12, s45
	s_add_u32 s0, s12, 0x400000
	s_addc_u32 s1, s13, 0
	s_lshl_b32 s24, s9, 6
	s_ashr_i32 s25, s24, 31
	s_lshl_b64 s[24:25], s[24:25], 4
	s_add_u32 s34, s34, s24
	s_addc_u32 s35, s31, s25
	s_lshl_b32 s24, s42, 4
	s_and_b64 s[26:27], s[26:27], exec
	s_cselect_b32 s9, s46, s13
	s_cselect_b32 s25, s45, s12
	s_and_b64 s[26:27], exec, s[16:17]
	v_mul_u32_u24_e32 v20, 0x2aab, v0
	s_cselect_b32 s8, s8, s24
	v_lshrrev_b32_e32 v156, 16, v20
	s_add_i32 s4, s4, s8
	s_lshl_b32 s8, s3, 2
	v_mul_lo_u16_e32 v20, 6, v156
	s_and_b32 s47, s8, 12
	v_sub_u16_e32 v20, v0, v20
	s_or_b32 s4, s4, s47
	v_lshlrev_b32_e32 v20, 2, v20
	v_lshl_or_b32 v24, s4, 6, v199
	global_load_dword v176, v20, s[14:15]
	v_mov_b32_e32 v20, s25
	v_mov_b32_e32 v21, s9
	v_ashrrev_i32_e32 v25, 31, v24
	v_mov_b32_e32 v167, 0
	v_lshlrev_b32_e32 v166, 4, v199
	v_lshl_add_u64 v[20:21], v[24:25], 4, v[20:21]
	s_mov_b32 s5, 0
	v_lshl_add_u64 v[18:19], s[34:35], 0, v[166:167]
	global_load_dwordx4 v[146:149], v[20:21], off
	global_load_dwordx4 v[138:141], v[20:21], off offset:1024
	global_load_dwordx4 v[24:27], v166, s[34:35]
	s_lshl_b32 s4, s20, 4
	v_lshl_add_u64 v[18:19], v[18:19], 0, s[4:5]
	global_load_dwordx4 v[28:31], v[18:19], off
	global_load_dwordx4 v[150:153], v[20:21], off offset:2048
	global_load_dwordx4 v[142:145], v[20:21], off offset:3072
	s_lshl_b32 s9, s21, 4
	s_and_b32 s8, s21, 64
	s_and_b32 s9, s9, 0xfffff800
	s_or_b32 s8, s8, s9
	v_or_b32_e32 v34, s8, v199
	v_lshl_add_u64 v[32:33], v[18:19], 0, s[4:5]
	v_ashrrev_i32_e32 v35, 31, v34
	global_load_dwordx4 v[18:21], v[32:33], off
	v_lshl_add_u64 v[32:33], v[32:33], 0, s[4:5]
	global_load_dwordx4 v[62:65], v[32:33], off
	v_lshlrev_b32_e32 v23, 3, v199
	s_mulk_i32 s3, 0x840
	v_or_b32_e32 v36, 0x100, v34
	v_ashrrev_i32_e32 v37, 31, v36
	v_lshl_add_u64 v[36:37], v[36:37], 4, s[0:1]
	global_load_dwordx4 v[122:125], v[36:37], off offset:-4096
	global_load_dwordx4 v[98:101], v[36:37], off offset:-2048
	global_load_dwordx4 v[114:117], v[36:37], off
	global_load_dwordx4 v[86:89], v[36:37], off offset:2048
	v_or_b32_e32 v38, 0x300, v34
	v_ashrrev_i32_e32 v39, 31, v38
	v_lshl_add_u64 v[38:39], v[38:39], 4, s[0:1]
	global_load_dwordx4 v[126:129], v[38:39], off offset:-4096
	global_load_dwordx4 v[90:93], v[38:39], off offset:-2048
	global_load_dwordx4 v[118:121], v[38:39], off
	global_load_dwordx4 v[78:81], v[38:39], off offset:2048
	v_or_b32_e32 v36, 0x500, v34
	v_ashrrev_i32_e32 v37, 31, v36
	v_lshl_add_u64 v[36:37], v[36:37], 4, s[0:1]
	global_load_dwordx4 v[102:105], v[36:37], off offset:-4096
	global_load_dwordx4 v[74:77], v[36:37], off offset:-2048
	global_load_dwordx4 v[106:109], v[36:37], off
	global_load_dwordx4 v[82:85], v[36:37], off offset:2048
	v_or_b32_e32 v38, 0x700, v34
	v_ashrrev_i32_e32 v39, 31, v38
	v_lshl_add_u64 v[38:39], v[38:39], 4, s[0:1]
	global_load_dwordx4 v[110:113], v[38:39], off offset:-4096
	global_load_dwordx4 v[94:97], v[38:39], off offset:-2048
	global_load_dwordx4 v[134:137], v[38:39], off
	global_load_dwordx4 v[130:133], v[38:39], off offset:2048
	v_add_u32_e32 v189, s3, v23
	v_and_b32_e32 v157, 31, v0
	v_lshlrev_b32_e32 v22, 4, v22
	s_movk_i32 s0, 0x210
	v_mad_u32_u24 v179, v157, s0, v22
	s_waitcnt vmcnt(21)
	v_pk_add_f16 v36, v24, v146
	v_pk_add_f16 v37, v25, v147
	s_waitcnt vmcnt(20)
	v_pk_add_f16 v23, v28, v146
	v_pk_mul_f16 v34, v26, v148 clamp
	v_pk_mul_f16 v35, v27, v149 clamp
	v_pk_max_f16 v34, v36, v34
	v_pk_max_f16 v35, v37, v35
	v_pk_add_f16 v38, v29, v147
	v_pk_add_f16 v40, v25, v139
	v_pk_mul_f16 v36, v30, v148 clamp
	v_pk_mul_f16 v37, v31, v149 clamp
	v_pk_max_f16 v36, v23, v36
	v_pk_max_f16 v37, v38, v37
	v_pk_add_f16 v23, v24, v138
	s_nop 0
	v_pk_mul_f16 v38, v26, v140 clamp
	v_pk_mul_f16 v39, v27, v141 clamp
	v_pk_max_f16 v38, v23, v38
	v_pk_max_f16 v39, v40, v39
	v_pk_add_f16 v23, v28, v138
	ds_write2_b64 v189, v[34:35], v[38:39] offset1:66
	v_pk_add_f16 v38, v29, v139
	s_nop 0
	v_pk_mul_f16 v34, v30, v140 clamp
	v_pk_mul_f16 v35, v31, v141 clamp
	v_pk_max_f16 v34, v23, v34
	v_pk_max_f16 v35, v38, v35
	v_add_u32_e32 v23, 0x4000, v189
	ds_write2_b64 v23, v[36:37], v[34:35] offset0:64 offset1:130
	s_waitcnt vmcnt(19)
	v_pk_add_f16 v23, v24, v150
	v_pk_add_f16 v36, v25, v151
	v_pk_add_f16 v38, v29, v151
	v_pk_mul_f16 v34, v26, v152 clamp
	v_pk_mul_f16 v35, v27, v153 clamp
	v_pk_max_f16 v34, v23, v34
	v_pk_max_f16 v35, v36, v35
	v_pk_add_f16 v23, v28, v150
	s_nop 0
	v_pk_mul_f16 v36, v30, v152 clamp
	v_pk_mul_f16 v37, v31, v153 clamp
	v_pk_max_f16 v36, v23, v36
	v_pk_max_f16 v37, v38, v37
	s_waitcnt vmcnt(18)
	v_pk_add_f16 v23, v24, v142
	v_pk_add_f16 v38, v25, v143
	s_nop 0
	v_pk_mul_f16 v24, v26, v144 clamp
	v_pk_mul_f16 v25, v27, v145 clamp
	v_pk_max_f16 v24, v23, v24
	v_pk_max_f16 v25, v38, v25
	v_pk_add_f16 v23, v28, v142
	ds_write2_b64 v189, v[34:35], v[24:25] offset0:132 offset1:198
	v_pk_add_f16 v26, v29, v143
	s_nop 0
	v_pk_mul_f16 v24, v30, v144 clamp
	v_pk_mul_f16 v25, v31, v145 clamp
	v_pk_max_f16 v24, v23, v24
	v_pk_max_f16 v25, v26, v25
	v_add_u32_e32 v23, 0x4400, v189
	v_lshl_add_u64 v[30:31], v[32:33], 0, s[4:5]
	ds_write2_b64 v23, v[36:37], v[24:25] offset0:68 offset1:134
	s_waitcnt lgkmcnt(0)
	s_barrier
	global_load_dwordx4 v[158:161], v[30:31], off
	ds_read_b128 v[22:25], v179
	ds_read_b128 v[26:29], v179 offset:32
	ds_read_b128 v[46:49], v179 offset:64
	ds_read_b128 v[50:53], v179 offset:96
	ds_read_b128 v[54:57], v179 offset:128
	ds_read_b128 v[58:61], v179 offset:160
	v_lshl_add_u64 v[154:155], v[30:31], 0, s[4:5]
	s_waitcnt vmcnt(16) lgkmcnt(5)
	v_mfma_f32_32x32x16_f16 v[30:45], v[122:125], v[22:25], v[2:17]
	ds_read_b128 v[162:165], v179 offset:192
	s_waitcnt vmcnt(15) lgkmcnt(5)
	v_mfma_f32_32x32x16_f16 v[30:45], v[98:101], v[26:29], v[30:45]
	ds_read_b128 v[22:25], v179 offset:224
	s_waitcnt vmcnt(14) lgkmcnt(5)
	v_mfma_f32_32x32x16_f16 v[30:45], v[114:117], v[46:49], v[30:45]
	ds_read_b128 v[26:29], v179 offset:256
	s_waitcnt vmcnt(13) lgkmcnt(5)
	v_mfma_f32_32x32x16_f16 v[30:45], v[86:89], v[50:53], v[30:45]
	ds_read_b128 v[46:49], v179 offset:288
	s_waitcnt vmcnt(12) lgkmcnt(5)
	v_mfma_f32_32x32x16_f16 v[30:45], v[126:129], v[54:57], v[30:45]
	ds_read_b128 v[50:53], v179 offset:320
	s_waitcnt vmcnt(11) lgkmcnt(5)
	v_mfma_f32_32x32x16_f16 v[30:45], v[90:93], v[58:61], v[30:45]
	ds_read_b128 v[54:57], v179 offset:352
	s_waitcnt vmcnt(10) lgkmcnt(5)
	v_mfma_f32_32x32x16_f16 v[30:45], v[118:121], v[162:165], v[30:45]
	ds_read_b128 v[58:61], v179 offset:384
	s_waitcnt vmcnt(9) lgkmcnt(5)
	v_mfma_f32_32x32x16_f16 v[30:45], v[78:81], v[22:25], v[30:45]
	ds_read_b128 v[162:165], v179 offset:416
	s_waitcnt vmcnt(8) lgkmcnt(5)
	v_mfma_f32_32x32x16_f16 v[30:45], v[102:105], v[26:29], v[30:45]
	ds_read_b128 v[22:25], v179 offset:448
	s_waitcnt vmcnt(7) lgkmcnt(5)
	v_mfma_f32_32x32x16_f16 v[30:45], v[74:77], v[46:49], v[30:45]
	ds_read_b128 v[26:29], v179 offset:480
	s_waitcnt vmcnt(6) lgkmcnt(5)
	v_mfma_f32_32x32x16_f16 v[30:45], v[106:109], v[50:53], v[30:45]
	s_waitcnt vmcnt(5) lgkmcnt(4)
	v_mfma_f32_32x32x16_f16 v[30:45], v[82:85], v[54:57], v[30:45]
	s_waitcnt vmcnt(4) lgkmcnt(3)
	v_mfma_f32_32x32x16_f16 v[30:45], v[110:113], v[58:61], v[30:45]
	v_pk_add_f16 v48, v18, v146
	v_pk_add_f16 v49, v19, v147
	s_nop 0
	v_pk_mul_f16 v46, v20, v148 clamp
	v_pk_mul_f16 v47, v21, v149 clamp
	v_pk_max_f16 v46, v48, v46
	v_pk_max_f16 v47, v49, v47
	ds_write_b64 v189, v[46:47] offset:33792
	s_waitcnt vmcnt(3) lgkmcnt(3)
	v_mfma_f32_32x32x16_f16 v[30:45], v[94:97], v[162:165], v[30:45]
	v_pk_add_f16 v48, v18, v138
	v_pk_add_f16 v49, v19, v139
	s_nop 0
	v_pk_mul_f16 v46, v20, v140 clamp
	v_pk_mul_f16 v47, v21, v141 clamp
	v_pk_max_f16 v46, v48, v46
	v_pk_max_f16 v47, v49, v47
	ds_write_b64 v189, v[46:47] offset:34320
	s_waitcnt vmcnt(2) lgkmcnt(3)
	v_mfma_f32_32x32x16_f16 v[30:45], v[134:137], v[22:25], v[30:45]
	v_pk_add_f16 v48, v18, v150
	v_pk_add_f16 v49, v19, v151
	s_nop 0
	v_pk_mul_f16 v46, v20, v152 clamp
	v_pk_mul_f16 v47, v21, v153 clamp
	v_pk_max_f16 v46, v48, v46
	v_pk_max_f16 v47, v49, v47
	ds_write_b64 v189, v[46:47] offset:34848
	s_waitcnt vmcnt(1) lgkmcnt(3)
	v_mfma_f32_32x32x16_f16 v[30:45], v[130:133], v[26:29], v[30:45]
	v_pk_add_f16 v22, v18, v142
	v_pk_add_f16 v23, v19, v143
	s_nop 0
	v_pk_mul_f16 v18, v20, v144 clamp
	v_pk_mul_f16 v19, v21, v145 clamp
	v_pk_max_f16 v18, v22, v18
	v_pk_max_f16 v19, v23, v19
	ds_write_b64 v189, v[18:19] offset:35376
	global_load_dwordx4 v[162:165], v[154:155], off
	ds_read_b128 v[46:49], v179 offset:16896
	ds_read_b128 v[50:53], v179 offset:16928
	ds_read_b128 v[54:57], v179 offset:16960
	ds_read_b128 v[58:61], v179 offset:16992
	ds_read_b128 v[168:171], v179 offset:17024
	ds_read_b128 v[172:175], v179 offset:17056
	s_nop 0
	v_cvt_pk_f16_f32 v167, v30, v31
	v_cvt_pk_f16_f32 v177, v32, v33
	s_waitcnt lgkmcnt(5)
	v_mfma_f32_32x32x16_f16 v[18:33], v[122:125], v[46:49], v[2:17]
	ds_read_b128 v[180:183], v179 offset:17088
	s_waitcnt lgkmcnt(5)
	v_mfma_f32_32x32x16_f16 v[18:33], v[98:101], v[50:53], v[18:33]
	ds_read_b128 v[184:187], v179 offset:17120
	v_exp_f16_e64 v46, v167 clamp
	v_exp_f16_e64 v47, v177 clamp
	v_exp_f16_sdwa v46, v167 clamp dst_sel:WORD_1 dst_unused:UNUSED_PRESERVE src0_sel:WORD_1
	v_exp_f16_sdwa v47, v177 clamp dst_sel:WORD_1 dst_unused:UNUSED_PRESERVE src0_sel:WORD_1
	s_nop 0
	s_waitcnt lgkmcnt(5)
	v_mfma_f32_32x32x16_f16 v[18:33], v[114:117], v[54:57], v[18:33]
	ds_read_b128 v[190:193], v179 offset:17152
	s_movk_i32 s0, 0x3dc5
	v_mov_b32_e32 v178, 0xbdc5
	v_pk_fma_f16 v47, v47, s0, v178 op_sel_hi:[1,0,0]
	v_pk_fma_f16 v46, v46, s0, v178 op_sel_hi:[1,0,0]
	v_pk_max_f16 v47, v177, v47
	v_pk_max_f16 v46, v167, v46
	s_waitcnt lgkmcnt(5)
	v_mfma_f32_32x32x16_f16 v[18:33], v[86:89], v[58:61], v[18:33]
	ds_read_b128 v[194:197], v179 offset:17184
	v_cvt_pk_f16_f32 v48, v34, v35
	v_cvt_pk_f16_f32 v49, v36, v37
	s_waitcnt lgkmcnt(5)
	v_mfma_f32_32x32x16_f16 v[18:33], v[126:129], v[168:171], v[18:33]
	ds_read_b128 v[34:37], v179 offset:17216
	v_exp_f16_e64 v50, v48 clamp
	v_exp_f16_e64 v51, v49 clamp
	v_exp_f16_sdwa v50, v48 clamp dst_sel:WORD_1 dst_unused:UNUSED_PRESERVE src0_sel:WORD_1
	v_exp_f16_sdwa v51, v49 clamp dst_sel:WORD_1 dst_unused:UNUSED_PRESERVE src0_sel:WORD_1
	s_nop 0
	s_waitcnt lgkmcnt(5)
	v_mfma_f32_32x32x16_f16 v[18:33], v[90:93], v[172:175], v[18:33]
	ds_read_b128 v[168:171], v179 offset:17248
	v_pk_fma_f16 v51, v51, s0, v178 op_sel_hi:[1,0,0]
	v_pk_fma_f16 v50, v50, s0, v178 op_sel_hi:[1,0,0]
	v_pk_max_f16 v49, v49, v51
	v_pk_max_f16 v48, v48, v50
	s_waitcnt lgkmcnt(5)
	v_mfma_f32_32x32x16_f16 v[18:33], v[118:121], v[180:183], v[18:33]
	ds_read_b128 v[172:175], v179 offset:17280
	v_cvt_pk_f16_f32 v167, v38, v39
	v_cvt_pk_f16_f32 v177, v40, v41
	v_mfma_f32_16x16x32_f16 v[58:61], v[70:73], v[46:49], 0
	s_waitcnt lgkmcnt(5)
	v_mfma_f32_32x32x16_f16 v[18:33], v[78:81], v[184:187], v[18:33]
	ds_read_b128 v[38:41], v179 offset:17312
	v_exp_f16_e64 v188, v167 clamp
	v_exp_f16_e64 v198, v177 clamp
	v_exp_f16_sdwa v188, v167 clamp dst_sel:WORD_1 dst_unused:UNUSED_PRESERVE src0_sel:WORD_1
	v_exp_f16_sdwa v198, v177 clamp dst_sel:WORD_1 dst_unused:UNUSED_PRESERVE src0_sel:WORD_1
	s_nop 0
	s_waitcnt lgkmcnt(5)
	v_mfma_f32_32x32x16_f16 v[18:33], v[102:105], v[190:193], v[18:33]
	ds_read_b128 v[180:183], v179 offset:17344
	v_pk_fma_f16 v184, v198, s0, v178 op_sel_hi:[1,0,0]
	s_nop 0
	v_pk_max_f16 v185, v177, v184
	v_pk_fma_f16 v177, v188, s0, v178 op_sel_hi:[1,0,0]
	s_nop 0
	v_pk_max_f16 v184, v167, v177
	s_waitcnt lgkmcnt(5)
	v_mfma_f32_32x32x16_f16 v[18:33], v[74:77], v[194:197], v[18:33]
	ds_read_b128 v[190:193], v179 offset:17376
	v_cvt_pk_f16_f32 v42, v42, v43
	v_cvt_pk_f16_f32 v43, v44, v45
	s_waitcnt lgkmcnt(5)
	v_mfma_f32_32x32x16_f16 v[18:33], v[106:109], v[34:37], v[18:33]
	v_exp_f16_e64 v44, v42 clamp
	v_exp_f16_e64 v45, v43 clamp
	v_exp_f16_sdwa v44, v42 clamp dst_sel:WORD_1 dst_unused:UNUSED_PRESERVE src0_sel:WORD_1
	v_exp_f16_sdwa v45, v43 clamp dst_sel:WORD_1 dst_unused:UNUSED_PRESERVE src0_sel:WORD_1
	s_nop 0
	s_waitcnt lgkmcnt(4)
	v_mfma_f32_32x32x16_f16 v[18:33], v[82:85], v[168:171], v[18:33]
	v_pk_fma_f16 v34, v45, s0, v178 op_sel_hi:[1,0,0]
	s_nop 0
	v_pk_max_f16 v187, v43, v34
	v_pk_fma_f16 v34, v44, s0, v178 op_sel_hi:[1,0,0]
	s_nop 0
	v_pk_max_f16 v186, v42, v34
	s_waitcnt lgkmcnt(3)
	v_mfma_f32_32x32x16_f16 v[18:33], v[110:113], v[172:175], v[18:33]
	v_pk_add_f16 v36, v62, v146
	v_pk_add_f16 v37, v63, v147
	s_nop 0
	v_pk_mul_f16 v34, v64, v148 clamp
	v_pk_mul_f16 v35, v65, v149 clamp
	v_pk_max_f16 v34, v36, v34
	v_pk_max_f16 v35, v37, v35
	ds_write_b64 v189, v[34:35] offset:50688
	v_mfma_f32_16x16x32_f16 v[58:61], v[66:69], v[184:187], v[58:61]
	s_waitcnt lgkmcnt(3)
	v_mfma_f32_32x32x16_f16 v[18:33], v[94:97], v[38:41], v[18:33]
	v_pk_add_f16 v36, v62, v138
	v_pk_add_f16 v37, v63, v139
	s_nop 0
	v_pk_mul_f16 v34, v64, v140 clamp
	v_pk_mul_f16 v35, v65, v141 clamp
	v_pk_max_f16 v34, v36, v34
	v_pk_max_f16 v35, v37, v35
	ds_write_b64 v189, v[34:35] offset:51216
	s_waitcnt lgkmcnt(3)
	v_mfma_f32_32x32x16_f16 v[18:33], v[134:137], v[180:183], v[18:33]
	v_pk_add_f16 v36, v62, v150
	v_pk_add_f16 v37, v63, v151
	s_nop 0
	v_pk_mul_f16 v34, v64, v152 clamp
	v_pk_mul_f16 v35, v65, v153 clamp
	v_pk_max_f16 v34, v36, v34
	v_pk_max_f16 v35, v37, v35
	ds_write_b64 v189, v[34:35] offset:51744
	s_waitcnt lgkmcnt(3)
	v_mfma_f32_32x32x16_f16 v[18:33], v[130:133], v[190:193], v[18:33]
	v_pk_add_f16 v36, v62, v142
	v_pk_add_f16 v37, v63, v143
	s_nop 0
	v_pk_mul_f16 v34, v64, v144 clamp
	v_pk_mul_f16 v35, v65, v145 clamp
	v_pk_max_f16 v34, v36, v34
	v_pk_max_f16 v35, v37, v35
	ds_write_b64 v189, v[34:35] offset:52272
	v_and_b32_e32 v157, 15, v199
	v_lshrrev_b32_e32 v1, 5, v199
	v_lshl_or_b32 v157, v1, 4, v157
	v_bfe_u32 v1, v199, 4, 1
	v_lshlrev_b32_e32 v1, 2, v1
	v_or_b32_e32 v178, s2, v157
	v_mul_lo_u32 v167, v178, 7
	v_add_u32_e32 v170, v167, v1
	v_mov_b32_e32 v34, 0x10800
	v_lshl_add_u32 v206, v170, 2, v34
	v_and_b32_e32 v34, 16, v199
	v_cmp_eq_u32_e64 s[0:1], 0, v34
	v_mov_b32_e32 v34, 0x10808
	v_lshl_add_u32 v34, v167, 2, v34
	v_or_b32_e32 v36, 3, v1
	v_mul_i32_i24_e32 v34, -6, v156
	v_mul_u32_u24_e32 v35, 7, v156
	v_cmp_gt_u32_e64 s[2:3], 6, v36
	v_lshlrev_b32_e32 v171, 2, v167
	v_lshlrev_b32_e32 v172, 2, v36
	s_mov_b32 s5, 0x10800
	v_add3_u32 v36, v171, v172, s5
	ds_write2_b32 v206, v58, v59 offset1:1
	s_and_saveexec_b64 s[2:3], s[0:1]
	ds_write2_b32 v206, v60, v61 offset0:2 offset1:3
	s_or_b64 exec, exec, s[2:3]
	s_sub_i32 s9, 0xff, s28
	s_mul_i32 s9, s9, s28
	s_not_b32 s25, s28
	s_ashr_i32 s9, s9, 1
	s_add_i32 s24, s24, s25
	s_add_i32 s24, s24, s9
	s_mul_i32 s8, s39, 0x1fc0
	s_ashr_i32 s9, s24, 31
	s_mul_hi_u32 s5, s39, 0x1fc0
	s_add_u32 s8, s8, s24
	s_addc_u32 s5, s5, s9
	s_mul_i32 s5, s5, 6
	s_mul_hi_u32 s9, s8, 6
	s_add_i32 s9, s9, s5
	v_add_u32_e32 v34, v34, v0
	s_cmpk_lt_u32 s21, 0xc0
	v_add_u32_e32 v173, v34, v35
	v_lshl_or_b32 v177, v34, 8, v156
	s_mul_i32 s8, s8, 6
	s_cselect_b64 s[24:25], -1, 0
	s_cmpk_gt_u32 s21, 0xbf
	s_waitcnt lgkmcnt(0)
	s_barrier
	s_cbranch_scc1 .LBB1_33
	s_andn2_b64 vcc, exec, s[6:7]
	s_mov_b64 s[6:7], -1
	s_cbranch_vccnz .LBB1_29
	s_movk_i32 s5, 0x60
	v_cmp_gt_u32_e32 vcc, s5, v0
	s_and_saveexec_b64 s[6:7], vcc
	s_cbranch_execz .LBB1_28
	v_lshlrev_b32_e32 v38, 2, v173
	v_add_u32_e32 v46, 0x10800, v38
	ds_read2_b32 v[34:35], v46 offset1:224
	v_add_u32_e32 v36, 0x700, v46
	ds_read2_b32 v[36:37], v36 offset1:224
	v_add_u32_e32 v39, 0x109c0, v38
	v_add_u32_e32 v40, 0x10d40, v38
	v_add_u32_e32 v41, 0x110c0, v38
	v_add_u32_e32 v42, 0x11440, v38
	v_add_u32_e32 v43, 0x117c0, v38
	v_add_u32_e32 v44, 0x11b40, v38
	v_add_u32_e32 v45, 0x11ec0, v38
	v_add_u32_e32 v47, 0x12240, v38
	ds_read_b32 v38, v39
	ds_read_b32 v39, v40
	ds_read_b32 v40, v41
	ds_read_b32 v41, v42
	ds_read_b32 v42, v43
	ds_read_b32 v43, v44
	ds_read_b32 v44, v45
	ds_read_b32 v45, v47
	s_waitcnt lgkmcnt(6)
	v_pk_add_f32 v[34:35], v[34:35], v[38:39]
	s_lshl_b64 s[26:27], s[8:9], 2
	v_add_f32_e32 v34, 0, v34
	v_add_f32_e32 v38, v34, v35
	s_waitcnt lgkmcnt(4)
	v_pk_add_f32 v[34:35], v[36:37], v[40:41]
	v_add_u32_e32 v36, 0xe00, v46
	ds_read2_b32 v[36:37], v36 offset1:224
	v_add_f32_e32 v34, v38, v34
	v_add_u32_e32 v38, 0x1500, v46
	ds_read2_b32 v[38:39], v38 offset1:224
	v_add_f32_e32 v40, v34, v35
	s_waitcnt lgkmcnt(1)
	v_pk_add_f32 v[34:35], v[36:37], v[42:43]
	s_add_u32 s26, s10, s26
	v_add_f32_e32 v34, v40, v34
	v_add_f32_e32 v36, v34, v35
	s_waitcnt lgkmcnt(0)
	v_pk_add_f32 v[34:35], v[38:39], v[44:45]
	s_addc_u32 s27, s11, s27
	v_add_f32_e32 v34, v36, v34
	v_add_f32_e32 v34, v34, v35
	v_fmamk_f32 v34, v34, 0x3eb17218, v176
	v_lshlrev_b32 v35, 2, v0
	global_store_dword v35, v34, s[26:27]
